# baseline (speedup 1.0000x reference)
_Z6gemm_kILi2ELi128ELi2ELi4EEv5GArgs:
	s_load_dwordx4 s[4:7], s[0:1], 0x38
	s_lshr_b32 s9, s2, 3
	s_and_b32 s3, s2, 7
	s_mul_hi_u32 s10, s9, 0x33333334
	s_mul_i32 s10, s10, 5
	s_waitcnt lgkmcnt(0)
	s_load_dword s8, s[6:7], 0x280
	s_sub_i32 s9, s9, s10
	s_waitcnt lgkmcnt(0)
	s_mul_i32 s3, s8, s3
	s_ashr_i32 s10, s3, 3
	s_add_i32 s3, s3, s8
	s_ashr_i32 s8, s3, 3
	s_add_i32 s3, s10, s9
	s_cmp_ge_i32 s3, s8
	s_cbranch_scc1 .LBB13_20
	s_lshl_b32 s8, s3, 2
	s_ashr_i32 s9, s8, 31
	s_lshl_b64 s[8:9], s[8:9], 2
	s_add_u32 s6, s6, s8
	s_addc_u32 s7, s7, s9
	s_load_dwordx4 s[12:15], s[6:7], 0x0
	s_mov_b32 s3, 0
	s_waitcnt lgkmcnt(0)
	s_cmp_lt_i32 s12, 0
	s_cbranch_scc1 .LBB13_20
	s_mov_b32 s8, s13
	s_mov_b32 s9, s14
	v_lshrrev_b32_e32 v1, 6, v0
	v_bfe_u32 v76, v0, 3, 3
	v_lshl_or_b32 v6, v1, 5, v76
	v_or_b32_e32 v44, 8, v6
	s_waitcnt lgkmcnt(0)
	s_add_i32 s6, s9, -1
	v_add_u32_e32 v4, s8, v6
	v_min_i32_e32 v2, s6, v4
	v_add_u32_e32 v4, 16, v4
	v_min_i32_e32 v4, s6, v4
	v_ashrrev_i32_e32 v3, 31, v2
	v_ashrrev_i32_e32 v5, 31, v4
	v_lshl_add_u64 v[2:3], v[2:3], 2, s[4:5]
	v_lshl_add_u64 v[4:5], v[4:5], 2, s[4:5]
	global_load_dword v7, v[2:3], off
	global_load_dword v8, v[4:5], off
	v_or_b32_e32 v4, 24, v6
	v_add_u32_e32 v2, s8, v4
	v_min_i32_e32 v2, s6, v2
	v_ashrrev_i32_e32 v3, 31, v2
	v_lshl_add_u64 v[2:3], v[2:3], 2, s[4:5]
	global_load_dword v9, v[2:3], off
	v_add_u32_e32 v2, s8, v44
	v_min_i32_e32 v2, s6, v2
	v_ashrrev_i32_e32 v3, 31, v2
	v_lshl_add_u64 v[2:3], v[2:3], 2, s[4:5]
	global_load_dword v45, v[2:3], off
	s_load_dwordx2 s[14:15], s[0:1], 0x0
	s_load_dwordx4 s[4:7], s[0:1], 0x10
	v_lshrrev_b32_e32 v4, 1, v4
	v_bfe_u32 v2, v0, 4, 2
	v_xor_b32_e32 v4, v4, v0
	s_mul_hi_u32 s10, s2, 0xcccccccd
	s_movk_i32 s2, 0x680
	v_bitop3_b32 v2, v2, v0, 7 bitop3:0x78
	s_waitcnt lgkmcnt(0)
	v_mov_b64_e32 v[36:37], s[14:15]
	v_lshlrev_b32_e32 v4, 3, v4
	v_mov_b32_e32 v3, 0
	v_bfe_u32 v77, v0, 5, 1
	s_lshl_b32 s10, s10, 2
	v_lshlrev_b32_e32 v2, 4, v2
	v_bitop3_b32 v11, v4, 8, 56 bitop3:0x6c
	s_mul_i32 s16, s12, 0x900000
	v_lshl_or_b32 v48, v1, 1, v77
	s_and_b32 s10, s10, 0xffffff80
	s_mul_hi_u32 s13, s12, 0x900000
	v_mul_u32_u24_e32 v10, 0x6000, v48
	s_add_u32 s4, s4, s16
	s_addc_u32 s5, s5, s13
	s_mov_b32 s11, s3
	v_and_b32_e32 v78, 31, v0
	s_movk_i32 s18, 0x3000
	s_movk_i32 s17, 0x6000
	s_mov_b32 s19, 0x9000
	s_mov_b32 s20, 0xc000
	s_mov_b32 s21, 0xf000
	s_mov_b32 s22, 0x12000
	v_lshlrev_b32_e32 v81, 12, v1
	v_or_b32_e32 v46, 0xc00, v81
	v_readfirstlane_b32 s13, v81
	s_mov_b32 m0, s13
	v_readfirstlane_b32 s16, v46
	v_lshlrev_b32_e32 v82, 9, v78
	s_load_dwordx2 s[0:1], s[0:1], 0x70
	v_lshrrev_b32_e32 v79, 7, v0
	v_bfe_u32 v80, v0, 6, 1
	v_lshlrev_b32_e32 v89, 13, v79
	v_lshlrev_b32_e32 v90, 7, v78
	v_lshlrev_b32_e32 v91, 13, v80
	s_mov_b32 s13, 0xc3000
	v_mov_b32_e32 v53, v3
	v_mov_b32_e32 v54, v3
	v_mov_b32_e32 v55, v3
	v_mov_b32_e32 v56, v3
	v_mov_b32_e32 v57, v3
	v_mov_b32_e32 v58, v3
	v_mov_b32_e32 v59, v3
	v_mov_b32_e32 v60, v3
	v_mov_b32_e32 v61, v3
	v_mov_b32_e32 v62, v3
	v_mov_b32_e32 v63, v3
	v_mov_b32_e32 v64, v3
	v_mov_b32_e32 v65, v3
	s_waitcnt vmcnt(3)
	v_mad_i64_i32 v[4:5], s[14:15], v7, s2, v[36:37]
	v_lshl_add_u64 v[66:67], v[4:5], 0, v[2:3]
	s_waitcnt vmcnt(2)
	v_mad_i64_i32 v[4:5], s[14:15], v8, s2, v[36:37]
	v_xor_b32_e32 v2, 16, v2
	v_lshl_add_u64 v[68:69], v[4:5], 0, v[2:3]
	s_waitcnt vmcnt(1)
	v_mad_i64_i32 v[6:7], s[14:15], v9, s2, v[36:37]
	v_lshlrev_b32_e32 v2, 1, v11
	v_lshl_add_u64 v[70:71], v[6:7], 0, v[2:3]
	v_lshlrev_b32_e32 v2, 2, v10
	v_lshl_add_u64 v[4:5], s[4:5], 0, v[2:3]
	v_lshlrev_b32_e32 v2, 4, v78
	v_lshl_add_u64 v[4:5], s[10:11], 2, v[4:5]
	v_lshl_add_u64 v[72:73], v[4:5], 0, v[2:3]
	v_add_co_u32_e32 v38, vcc, s18, v72
	s_mov_b32 s4, 0x15000
	s_nop 0
	v_addc_co_u32_e32 v39, vcc, 0, v73, vcc
	v_add_co_u32_e32 v40, vcc, s17, v72
	v_lshrrev_b32_e32 v2, 2, v0
	s_nop 0
	v_addc_co_u32_e32 v41, vcc, 0, v73, vcc
	v_add_co_u32_e32 v12, vcc, s19, v72
	s_mov_b32 s11, 1
	s_nop 0
	v_addc_co_u32_e32 v13, vcc, 0, v73, vcc
	v_add_co_u32_e32 v14, vcc, s20, v72
	s_mov_b32 s17, 0xcf000
	s_nop 0
	v_addc_co_u32_e32 v15, vcc, 0, v73, vcc
	v_add_co_u32_e32 v20, vcc, s21, v72
	global_load_dwordx4 v[4:7], v[12:13], off
	global_load_dwordx4 v[8:11], v[14:15], off
	v_addc_co_u32_e32 v21, vcc, 0, v73, vcc
	v_add_co_u32_e32 v22, vcc, s22, v72
	s_mov_b32 s18, 0xd2000
	s_nop 0
	v_addc_co_u32_e32 v23, vcc, 0, v73, vcc
	v_add_co_u32_e32 v42, vcc, s4, v72
	global_load_dwordx4 v[12:15], v[20:21], off
	global_load_dwordx4 v[16:19], v[22:23], off
	v_addc_co_u32_e32 v43, vcc, 0, v73, vcc
	global_load_dwordx4 v[20:23], v[42:43], off
	global_load_dwordx4 v[24:27], v[38:39], off
	global_load_dwordx4 v[28:31], v[40:41], off
	global_load_dwordx4 v[32:35], v[72:73], off
	v_lshlrev_b32_e32 v40, 1, v0
	v_bfe_u32 v38, v0, 2, 1
	v_lshlrev_b32_e32 v41, 2, v78
	v_and_b32_e32 v40, 6, v40
	v_bitop3_b32 v38, v38, v48, v40 bitop3:0x36
	v_or_b32_e32 v40, 2, v41
	v_or_b32_e32 v49, 3, v41
	v_lshrrev_b32_e32 v41, 1, v44
	v_lshlrev_b32_e32 v83, 4, v38
	v_bfe_u32 v38, v40, 1, 3
	v_lshlrev_b32_e32 v84, 7, v40
	v_xor_b32_e32 v40, v41, v0
	v_or_b32_e32 v42, 0x400, v81
	v_bitop3_b32 v38, v2, v38, 1 bitop3:0x6c
	v_lshlrev_b32_e32 v40, 4, v40
	v_mov_b32_e32 v39, v3
	v_or_b32_e32 v43, 0x800, v81
	v_readfirstlane_b32 s14, v42
	v_xor_b32_e32 v41, v38, v48
	v_and_b32_e32 v38, 0x70, v40
	s_waitcnt vmcnt(8)
	v_mad_i64_i32 v[36:37], s[4:5], v45, s2, v[36:37]
	v_readfirstlane_b32 s15, v43
	v_lshl_add_u64 v[74:75], v[36:37], 0, v[38:39]
	global_load_lds_dwordx4 v[66:67], off
	s_mov_b32 m0, s14
	v_bfe_u32 v50, v49, 1, 3
	global_load_lds_dwordx4 v[74:75], off
	s_mov_b32 m0, s15
	v_bitop3_b32 v2, v2, v50, 1 bitop3:0x6c
	global_load_lds_dwordx4 v[68:69], off
	s_mov_b32 m0, s16
	v_xor_b32_e32 v2, v2, v48
	global_load_lds_dwordx4 v[70:71], off
	v_readfirstlane_b32 s40, v81
	s_mov_b64 s[44:45], 0x3000
	s_mov_b64 s[46:47], 0x6000
	s_mov_b64 s[48:49], 0x9000
	s_mov_b64 s[50:51], 0xc000
	s_mov_b64 s[52:53], 0xf000
	s_mov_b64 s[54:55], 0x12000
	s_mov_b64 s[56:57], 0x15000
	s_mov_b32 s41, 0
	s_mov_b32 s42, 0x4000
	s_mov_b32 s43, 0x8000
	s_movk_i32 s2, 0x80
	s_add_i32 s23, s40, s42
	v_lshl_add_u64 v[144:145], v[66:67], 0, s[2:3]
	s_mov_b32 m0, s23
	s_add_i32 s23, s23, 0x400
	global_load_lds_dwordx4 v[144:145], off
	v_lshl_add_u64 v[144:145], v[74:75], 0, s[2:3]
	s_mov_b32 m0, s23
	s_add_i32 s23, s23, 0x400
	global_load_lds_dwordx4 v[144:145], off
	v_lshl_add_u64 v[144:145], v[68:69], 0, s[2:3]
	s_mov_b32 m0, s23
	s_add_i32 s23, s23, 0x400
	global_load_lds_dwordx4 v[144:145], off
	v_lshl_add_u64 v[144:145], v[70:71], 0, s[2:3]
	s_mov_b32 m0, s23
	s_nop 0
	global_load_lds_dwordx4 v[144:145], off
	s_mov_b32 s22, 0xc0000
	s_mov_b32 s23, 0
	v_lshl_add_u64 v[176:177], v[72:73], 0, s[22:23]
	v_lshl_add_u64 v[178:179], v[176:177], 0, s[44:45]
	v_lshl_add_u64 v[180:181], v[176:177], 0, s[46:47]
	v_lshl_add_u64 v[182:183], v[176:177], 0, s[48:49]
	v_lshl_add_u64 v[184:185], v[176:177], 0, s[50:51]
	v_lshl_add_u64 v[186:187], v[176:177], 0, s[52:53]
	v_lshl_add_u64 v[188:189], v[176:177], 0, s[54:55]
	v_lshl_add_u64 v[190:191], v[176:177], 0, s[56:57]
	global_load_dwordx4 v[144:147], v[176:177], off
	global_load_dwordx4 v[148:151], v[178:179], off
	global_load_dwordx4 v[152:155], v[180:181], off
	global_load_dwordx4 v[156:159], v[182:183], off
	global_load_dwordx4 v[160:163], v[184:185], off
	global_load_dwordx4 v[164:167], v[186:187], off
	global_load_dwordx4 v[168:171], v[188:189], off
	global_load_dwordx4 v[172:175], v[190:191], off
	v_lshlrev_b32_e32 v86, 4, v2
	v_lshlrev_b32_e32 v87, 7, v49
	v_or_b32_e32 v51, v82, v83
	v_lshlrev_b32_e32 v85, 4, v41
	v_add_u32_e32 v2, v87, v86
	v_add_u32_e32 v52, v84, v85
	s_mov_b64 s[4:5], 0x80
	s_mov_b32 s14, 0xc6000
	s_mov_b32 s15, 0xc9000
	s_mov_b32 s16, 0xcc000
	s_mov_b32 s19, 0xd5000
	s_mov_b32 s21, 0
	s_mov_b32 s20, 0
	v_mov_b32_e32 v48, v3
	v_mov_b32_e32 v49, v3
	v_mov_b32_e32 v50, v3
	s_waitcnt vmcnt(12)
	v_cvt_pk_f16_f32 v38, v8, v12
	v_cvt_pk_f16_f32 v39, v16, v20
	v_cvt_pk_f16_f32 v42, v9, v13
	v_cvt_pk_f16_f32 v37, v28, v4
	v_cvt_pk_f16_f32 v36, v32, v24
	v_cvt_pk_f16_f32 v45, v30, v6
	v_cvt_pk_f16_f32 v9, v19, v23
	v_cvt_pk_f16_f32 v8, v11, v15
	v_cvt_pk_f16_f32 v7, v31, v7
	v_cvt_pk_f16_f32 v6, v35, v27
	v_cvt_pk_f16_f32 v43, v17, v21
	v_cvt_pk_f16_f32 v41, v29, v5
	v_cvt_pk_f16_f32 v40, v33, v25
	v_cvt_pk_f16_f32 v47, v18, v22
	v_cvt_pk_f16_f32 v46, v10, v14
	v_cvt_pk_f16_f32 v44, v34, v26
	ds_write_b128 v51, v[36:39] offset:49152
	ds_write_b128 v51, v[40:43] offset:49280
	ds_write_b128 v52, v[44:47] offset:49152
	ds_write_b128 v2, v[6:9] offset:49152
	v_lshrrev_b32_e32 v2, 1, v0
	v_bfe_u32 v4, v0, 4, 1
	v_bitop3_b32 v2, v2, v4, 7 bitop3:0x6c
	v_xor_b32_e32 v4, v2, v77
	v_lshlrev_b32_e32 v88, 4, v4
	v_or_b32_e32 v4, 2, v77
	v_xor_b32_e32 v4, v2, v4
	v_lshlrev_b32_e32 v92, 4, v4
	v_or_b32_e32 v4, 4, v77
	v_xor_b32_e32 v4, v2, v4
	s_waitcnt vmcnt(12)
	v_lshlrev_b32_e32 v93, 4, v4
	v_or_b32_e32 v4, 6, v77
	v_xor_b32_e32 v2, v2, v4
	v_lshlrev_b32_e32 v94, 4, v2
	v_mov_b32_e32 v2, v3
	v_mov_b32_e32 v4, v3
	v_mov_b32_e32 v5, v3
	v_mov_b32_e32 v6, v3
	v_mov_b32_e32 v7, v3
	v_mov_b32_e32 v8, v3
	v_mov_b32_e32 v9, v3
	v_mov_b32_e32 v10, v3
	v_mov_b32_e32 v11, v3
	v_mov_b32_e32 v12, v3
	v_mov_b32_e32 v13, v3
	v_mov_b32_e32 v14, v3
	v_mov_b32_e32 v15, v3
	v_mov_b32_e32 v16, v3
	v_mov_b32_e32 v17, v3
	v_mov_b32_e32 v18, v3
	v_mov_b32_e32 v19, v3
	v_mov_b32_e32 v20, v3
	v_mov_b32_e32 v21, v3
	v_mov_b32_e32 v22, v3
	v_mov_b32_e32 v23, v3
	v_mov_b32_e32 v24, v3
	v_mov_b32_e32 v25, v3
	v_mov_b32_e32 v26, v3
	v_mov_b32_e32 v27, v3
	v_mov_b32_e32 v28, v3
	v_mov_b32_e32 v29, v3
	v_mov_b32_e32 v30, v3
	v_mov_b32_e32 v31, v3
	v_mov_b32_e32 v32, v3
	v_mov_b32_e32 v33, v3
	v_mov_b32_e32 v34, v3
	v_mov_b32_e32 v35, v3
	v_mov_b32_e32 v36, v3
	v_mov_b32_e32 v37, v3
	v_mov_b32_e32 v38, v3
	v_mov_b32_e32 v39, v3
	v_mov_b32_e32 v40, v3
	v_mov_b32_e32 v41, v3
	v_mov_b32_e32 v42, v3
	v_mov_b32_e32 v43, v3
	v_mov_b32_e32 v44, v3
	v_mov_b32_e32 v45, v3
	v_mov_b32_e32 v46, v3
	v_mov_b32_e32 v47, v3
	v_mov_b32_e32 v51, v3
	v_mov_b32_e32 v52, v3
	s_waitcnt lgkmcnt(0)
	s_barrier
